# baseline (speedup 1.0000x reference)
_Z10agg_kernelPKjPKiPKDF16_S4_PKfS4_S0_S2_S2_S2_S2_Pf:
	s_and_b32 s3, s2, 1
	s_lshr_b32 s4, s2, 1
	s_load_dwordx16 s[8:23], s[0:1], 0x0
	s_load_dwordx8 s[24:31], s[0:1], 0x40
	s_mul_i32 s6, s4, 0xc4
	s_sub_u32 s5, 0xc350, s6
	s_min_u32 s5, s5, 0xc4
	v_lshrrev_b32_e32 v2, 2, v0
	v_and_b32_e32 v1, 3, v0
	v_lshrrev_b32_e32 v13, 1, v1
	v_lshl_add_u32 v13, s3, 1, v13
	v_lshlrev_b32_e32 v13, 2, v13
	v_lshlrev_b32_e32 v1, 4, v1
	s_lshl_b32 s52, s4, 2
	s_waitcnt lgkmcnt(0)
	s_add_u32 s52, s10, s52
	s_addc_u32 s53, s11, 0
	s_load_dwordx2 s[32:33], s[52:53], 0x0
	s_load_dwordx2 s[36:37], s[52:53], 0x404
	v_add_u32_e32 v40, s6, v2
	v_min_u32_e32 v40, 0xc34f, v40
	v_lshlrev_b32_e32 v40, 6, v40
	v_add3_u32 v40, v40, v13, 16
	global_load_dword v3, v40, s[16:17]
	global_load_dword v4, v40, s[16:17] offset:32
	v_lshlrev_b32_e32 v62, 2, v0
	v_mov_b32_e32 v63, 0
	ds_write_b32 v62, v63 offset:21248
	v_cmp_gt_u32_e32 vcc, 0x200, v0
	s_and_saveexec_b64 s[60:61], vcc
	ds_write_b32 v62, v63 offset:25344
	s_mov_b64 exec, s[60:61]
	s_waitcnt lgkmcnt(0)
	s_sub_u32 s38, s33, s32
	s_sub_u32 s39, s37, s36
	s_lshl_b32 s52, s32, 2
	s_add_u32 s42, s8, s52
	s_addc_u32 s43, s9, 0
	s_add_u32 s52, s36, 0xc3500
	s_lshl_b32 s52, s52, 2
	s_add_u32 s44, s8, s52
	s_addc_u32 s45, s9, 0
	s_max_i32 s52, s38, 1
	s_sub_u32 s52, s52, 1
	s_max_i32 s53, s39, 1
	s_sub_u32 s53, s53, 1
	s_movk_i32 s46, 0x80
	s_movk_i32 s55, 0x62
	s_movk_i32 s47, 0x61a8
	v_min_u32_e32 v41, s52, v0
	v_lshlrev_b32_e32 v41, 2, v41
	global_load_dword v8, v41, s[42:43]
	v_min_u32_e32 v41, s53, v0
	v_lshlrev_b32_e32 v41, 2, v41
	global_load_dword v24, v41, s[44:45]
	v_add_u32_e32 v40, 0x400, v0
	v_min_u32_e32 v41, s52, v40
	v_lshlrev_b32_e32 v41, 2, v41
	global_load_dword v9, v41, s[42:43]
	v_min_u32_e32 v41, s53, v40
	v_lshlrev_b32_e32 v41, 2, v41
	global_load_dword v25, v41, s[44:45]
	v_add_u32_e32 v40, 0x800, v0
	v_min_u32_e32 v41, s52, v40
	v_lshlrev_b32_e32 v41, 2, v41
	global_load_dword v10, v41, s[42:43]
	v_min_u32_e32 v41, s53, v40
	v_lshlrev_b32_e32 v41, 2, v41
	global_load_dword v26, v41, s[44:45]
	v_add_u32_e32 v40, 0xc00, v0
	v_min_u32_e32 v41, s52, v40
	v_lshlrev_b32_e32 v41, 2, v41
	global_load_dword v11, v41, s[42:43]
	v_min_u32_e32 v41, s53, v40
	v_lshlrev_b32_e32 v41, 2, v41
	global_load_dword v27, v41, s[44:45]
	v_mov_b32_e32 v61, 1
	v_mov_b32_e32 v43, 0xc4
	s_barrier
	s_waitcnt vmcnt(7)
	v_bfe_u32 v28, v8, 16, 7
	v_bfe_u32 v42, v8, 23, 1
	v_and_b32_e32 v44, 0xffff, v8
	v_mad_u32_u24 v28, v42, s55, v28
	v_cmp_le_u32_e32 vcc, s47, v44
	v_lshlrev_b32_e32 v28, 2, v28
	s_nop 0
	v_cndmask_b32_e32 v42, 0, v43, vcc
	v_lshl_add_u32 v28, v42, 2, v28
	v_cmp_gt_u32_e32 vcc, s38, v0
	s_and_saveexec_b64 s[60:61], vcc
	ds_add_rtn_u32 v16, v28, v61 offset:21248
	s_mov_b64 exec, s[60:61]
	s_waitcnt vmcnt(6)
	v_bfe_u32 v32, v24, 16, 7
	v_bfe_u32 v42, v24, 23, 1
	v_and_b32_e32 v44, 0xffff, v24
	v_mad_u32_u24 v32, v42, s55, v32
	v_cmp_le_u32_e32 vcc, s47, v44
	v_lshlrev_b32_e32 v32, 2, v32
	s_nop 0
	v_cndmask_b32_e32 v42, 0, v43, vcc
	v_lshl_add_u32 v32, v42, 2, v32
	v_cmp_gt_u32_e32 vcc, s39, v0
	s_and_saveexec_b64 s[60:61], vcc
	ds_add_rtn_u32 v20, v32, v61 offset:23296
	s_mov_b64 exec, s[60:61]
	s_waitcnt vmcnt(5)
	v_add_u32_e32 v40, 0x400, v0
	v_bfe_u32 v29, v9, 16, 7
	v_bfe_u32 v42, v9, 23, 1
	v_and_b32_e32 v44, 0xffff, v9
	v_mad_u32_u24 v29, v42, s55, v29
	v_cmp_le_u32_e32 vcc, s47, v44
	v_lshlrev_b32_e32 v29, 2, v29
	s_nop 0
	v_cndmask_b32_e32 v42, 0, v43, vcc
	v_lshl_add_u32 v29, v42, 2, v29
	v_cmp_gt_u32_e32 vcc, s38, v40
	s_and_saveexec_b64 s[60:61], vcc
	ds_add_rtn_u32 v17, v29, v61 offset:21248
	s_mov_b64 exec, s[60:61]
	s_waitcnt vmcnt(4)
	v_bfe_u32 v33, v25, 16, 7
	v_bfe_u32 v42, v25, 23, 1
	v_and_b32_e32 v44, 0xffff, v25
	v_mad_u32_u24 v33, v42, s55, v33
	v_cmp_le_u32_e32 vcc, s47, v44
	v_lshlrev_b32_e32 v33, 2, v33
	s_nop 0
	v_cndmask_b32_e32 v42, 0, v43, vcc
	v_lshl_add_u32 v33, v42, 2, v33
	v_cmp_gt_u32_e32 vcc, s39, v40
	s_and_saveexec_b64 s[60:61], vcc
	ds_add_rtn_u32 v21, v33, v61 offset:23296
	s_mov_b64 exec, s[60:61]
	s_waitcnt vmcnt(3)
	v_add_u32_e32 v40, 0x800, v0
	v_bfe_u32 v30, v10, 16, 7
	v_bfe_u32 v42, v10, 23, 1
	v_and_b32_e32 v44, 0xffff, v10
	v_mad_u32_u24 v30, v42, s55, v30
	v_cmp_le_u32_e32 vcc, s47, v44
	v_lshlrev_b32_e32 v30, 2, v30
	s_nop 0
	v_cndmask_b32_e32 v42, 0, v43, vcc
	v_lshl_add_u32 v30, v42, 2, v30
	v_cmp_gt_u32_e32 vcc, s38, v40
	s_and_saveexec_b64 s[60:61], vcc
	ds_add_rtn_u32 v18, v30, v61 offset:21248
	s_mov_b64 exec, s[60:61]
	s_waitcnt vmcnt(2)
	v_bfe_u32 v34, v26, 16, 7
	v_bfe_u32 v42, v26, 23, 1
	v_and_b32_e32 v44, 0xffff, v26
	v_mad_u32_u24 v34, v42, s55, v34
	v_cmp_le_u32_e32 vcc, s47, v44
	v_lshlrev_b32_e32 v34, 2, v34
	s_nop 0
	v_cndmask_b32_e32 v42, 0, v43, vcc
	v_lshl_add_u32 v34, v42, 2, v34
	v_cmp_gt_u32_e32 vcc, s39, v40
	s_and_saveexec_b64 s[60:61], vcc
	ds_add_rtn_u32 v22, v34, v61 offset:23296
	s_mov_b64 exec, s[60:61]
	s_waitcnt vmcnt(1)
	v_add_u32_e32 v40, 0xc00, v0
	v_bfe_u32 v31, v11, 16, 7
	v_bfe_u32 v42, v11, 23, 1
	v_and_b32_e32 v44, 0xffff, v11
	v_mad_u32_u24 v31, v42, s55, v31
	v_cmp_le_u32_e32 vcc, s47, v44
	v_lshlrev_b32_e32 v31, 2, v31
	s_nop 0
	v_cndmask_b32_e32 v42, 0, v43, vcc
	v_lshl_add_u32 v31, v42, 2, v31
	v_cmp_gt_u32_e32 vcc, s38, v40
	s_and_saveexec_b64 s[60:61], vcc
	ds_add_rtn_u32 v19, v31, v61 offset:21248
	s_mov_b64 exec, s[60:61]
	s_waitcnt vmcnt(0)
	v_bfe_u32 v35, v27, 16, 7
	v_bfe_u32 v42, v27, 23, 1
	v_and_b32_e32 v44, 0xffff, v27
	v_mad_u32_u24 v35, v42, s55, v35
	v_cmp_le_u32_e32 vcc, s47, v44
	v_lshlrev_b32_e32 v35, 2, v35
	s_nop 0
	v_cndmask_b32_e32 v42, 0, v43, vcc
	v_lshl_add_u32 v35, v42, 2, v35
	v_cmp_gt_u32_e32 vcc, s39, v40
	s_and_saveexec_b64 s[60:61], vcc
	ds_add_rtn_u32 v23, v35, v61 offset:23296
	s_mov_b64 exec, s[60:61]
	s_waitcnt lgkmcnt(0)
	s_barrier
	ds_read_b32 v40, v62 offset:21248
	v_and_b32_e32 v44, 63, v0
	v_lshrrev_b32_e32 v45, 6, v0
	v_lshlrev_b32_e32 v45, 2, v45
	v_and_b32_e32 v52, 0x1ff, v0
	v_lshrrev_b32_e32 v51, 9, v0
	v_cmp_le_u32_e32 vcc, 0xc4, v52
	v_mov_b32_e32 v47, 31
	s_nop 0
	v_cndmask_b32_e64 v53, 0, 1, vcc
	v_mul_u32_u24_e32 v54, 0xc4, v53
	v_sub_u32_e32 v54, v52, v54
	v_lshl_add_u32 v53, v51, 1, v53
	s_waitcnt lgkmcnt(0)
	v_min_u32_e32 v55, 31, v40
	v_sub_u32_e32 v55, v47, v55
	v_and_b32_e32 v47, 3, v0
	v_lshl_or_b32 v55, v55, 2, v47
	v_lshl_add_u32 v55, v53, 7, v55
	v_lshlrev_b32_e32 v55, 2, v55
	v_cmp_gt_u32_e32 vcc, 0x188, v52
	s_and_saveexec_b64 s[60:61], vcc
	ds_add_rtn_u32 v51, v55, v61 offset:25344
	s_mov_b64 exec, s[60:61]
	v_mov_b32_e32 v41, v40
	s_nop 1
	v_add_u32_dpp v41, v41, v41 row_shr:1 row_mask:0xf bank_mask:0xf
	s_nop 1
	v_add_u32_dpp v41, v41, v41 row_shr:2 row_mask:0xf bank_mask:0xf
	s_nop 1
	v_add_u32_dpp v41, v41, v41 row_shr:4 row_mask:0xf bank_mask:0xf
	s_nop 1
	v_add_u32_dpp v41, v41, v41 row_shr:8 row_mask:0xf bank_mask:0xf
	s_nop 1
	v_add_u32_dpp v41, v41, v41 row_bcast:15 row_mask:0xa bank_mask:0xf
	s_nop 1
	v_add_u32_dpp v41, v41, v41 row_bcast:31 row_mask:0xc bank_mask:0xf
	v_cmp_eq_u32_e32 vcc, 63, v44
	s_and_saveexec_b64 s[60:61], vcc
	ds_write_b32 v45, v41 offset:21056
	s_mov_b64 exec, s[60:61]
	s_waitcnt lgkmcnt(0)
	s_barrier
	v_cmp_gt_u32_e32 vcc, 0x200, v0
	s_and_saveexec_b64 s[60:61], vcc
	s_cbranch_execz .Lagg_bins_done
	ds_read_b32 v48, v62 offset:25344
	s_waitcnt lgkmcnt(0)
	v_mov_b32_e32 v49, v48
	s_nop 1
	v_add_u32_dpp v49, v49, v49 row_shr:1 row_mask:0xf bank_mask:0xf
	s_nop 1
	v_add_u32_dpp v49, v49, v49 row_shr:2 row_mask:0xf bank_mask:0xf
	s_nop 1
	v_add_u32_dpp v49, v49, v49 row_shr:4 row_mask:0xf bank_mask:0xf
	s_nop 1
	v_add_u32_dpp v49, v49, v49 row_shr:8 row_mask:0xf bank_mask:0xf
	s_nop 1
	v_add_u32_dpp v49, v49, v49 row_bcast:15 row_mask:0xa bank_mask:0xf
	s_nop 1
	v_add_u32_dpp v49, v49, v49 row_bcast:31 row_mask:0xc bank_mask:0xf
	s_nop 0
	v_sub_u32_e32 v50, v49, v48
	ds_write_b32 v62, v50 offset:29440
	v_cmp_eq_u32_e32 vcc, 63, v44
	s_and_b64 exec, exec, vcc
	ds_write_b32 v45, v49 offset:33536

.Lagg_w0_done:
	s_mov_b64 exec, s[60:61]
	s_waitcnt lgkmcnt(0)
	s_barrier
	ds_read_b32 v46, v45 offset:21120
	v_mov_b32_e32 v47, 0
	ds_read_b32 v48, v47 offset:21212
	ds_read_b32 v49, v47 offset:21244
	ds_read_b32 v50, v55 offset:29440
	v_lshlrev_b32_e32 v44, 3, v53
	ds_read_b32 v44, v44 offset:33536
	v_sub_u32_e32 v41, v41, v40
	v_mul_u32_u24_e32 v47, 0xc4, v53
	s_waitcnt lgkmcnt(0)
	v_add_u32_e32 v41, v41, v46
	ds_write_b32 v62, v41 offset:14336
	v_and_b32_e32 v46, 0x100, v55
	v_cmp_ne_u32_e32 vcc, 0, v46
	s_nop 1
	v_cndmask_b32_e32 v44, 0, v44, vcc
	v_add_u32_e32 v50, v50, v44
	v_add_u32_e32 v50, v50, v51
	v_add_lshl_u32 v50, v50, v47, 1
	v_cmp_gt_u32_e32 vcc, 0x188, v52
	s_and_saveexec_b64 s[60:61], vcc
	ds_write_b16 v50, v54 offset:18432
	s_mov_b64 exec, s[60:61]
	v_max_u32_e32 v48, v48, v49
	s_nop 0
	v_readfirstlane_b32 s52, v48
	s_max_u32 s52, s52, s38
	s_max_u32 s52, s52, s39
	s_cmpk_le_u32 s52, 0xe00
	s_cselect_b32 s7, 1, 0
	s_waitcnt lgkmcnt(0)
	s_barrier
	s_cmp_eq_u32 s7, 0
	s_cbranch_scc1 .Lagg_scatter_done
	ds_read_b32 v48, v28 offset:14336
	ds_read_b32 v49, v29 offset:14336
	ds_read_b32 v50, v30 offset:14336
	ds_read_b32 v51, v31 offset:14336
	s_waitcnt lgkmcnt(3)
	v_add_u32_e32 v48, v48, v16
	v_lshlrev_b32_e32 v48, 1, v48
	s_waitcnt lgkmcnt(2)
	v_add_u32_e32 v49, v49, v17
	v_lshlrev_b32_e32 v49, 1, v49
	s_waitcnt lgkmcnt(1)
	v_add_u32_e32 v50, v50, v18
	v_lshlrev_b32_e32 v50, 1, v50
	s_waitcnt lgkmcnt(0)
	v_add_u32_e32 v51, v51, v19
	v_lshlrev_b32_e32 v51, 1, v51
	v_cmp_gt_u32_e32 vcc, s38, v0
	s_and_saveexec_b64 s[60:61], vcc
	ds_write_b16 v48, v8 offset:0
	s_mov_b64 exec, s[60:61]
	v_add_u32_e32 v40, 0x400, v0
	v_cmp_gt_u32_e32 vcc, s38, v40
	s_and_saveexec_b64 s[60:61], vcc
	ds_write_b16 v49, v9 offset:0
	s_mov_b64 exec, s[60:61]
	v_add_u32_e32 v40, 0x800, v0
	v_cmp_gt_u32_e32 vcc, s38, v40
	s_and_saveexec_b64 s[60:61], vcc
	ds_write_b16 v50, v10 offset:0
	s_mov_b64 exec, s[60:61]
	v_add_u32_e32 v40, 0xc00, v0
	v_cmp_gt_u32_e32 vcc, s38, v40
	s_and_saveexec_b64 s[60:61], vcc
	ds_write_b16 v51, v11 offset:0
	s_mov_b64 exec, s[60:61]
	ds_read_b32 v48, v32 offset:16384
	ds_read_b32 v49, v33 offset:16384
	ds_read_b32 v50, v34 offset:16384
	ds_read_b32 v51, v35 offset:16384
	s_waitcnt lgkmcnt(3)
	v_add_u32_e32 v48, v48, v20
	v_lshlrev_b32_e32 v48, 1, v48
	s_waitcnt lgkmcnt(2)
	v_add_u32_e32 v49, v49, v21
	v_lshlrev_b32_e32 v49, 1, v49
	s_waitcnt lgkmcnt(1)
	v_add_u32_e32 v50, v50, v22
	v_lshlrev_b32_e32 v50, 1, v50
	s_waitcnt lgkmcnt(0)
	v_add_u32_e32 v51, v51, v23
	v_lshlrev_b32_e32 v51, 1, v51
	v_cmp_gt_u32_e32 vcc, s39, v0
	s_and_saveexec_b64 s[60:61], vcc
	ds_write_b16 v48, v24 offset:7168
	s_mov_b64 exec, s[60:61]
	v_add_u32_e32 v40, 0x400, v0
	v_cmp_gt_u32_e32 vcc, s39, v40
	s_and_saveexec_b64 s[60:61], vcc
	ds_write_b16 v49, v25 offset:7168
	s_mov_b64 exec, s[60:61]
	v_add_u32_e32 v40, 0x800, v0
	v_cmp_gt_u32_e32 vcc, s39, v40
	s_and_saveexec_b64 s[60:61], vcc
	ds_write_b16 v50, v26 offset:7168
	s_mov_b64 exec, s[60:61]
	v_add_u32_e32 v40, 0xc00, v0
	v_cmp_gt_u32_e32 vcc, s39, v40
	s_and_saveexec_b64 s[60:61], vcc
	ds_write_b16 v51, v27 offset:7168
	s_mov_b64 exec, s[60:61]
